# speedup vs baseline: 1.0111x; 1.0015x over previous
_Z7gemm128ILi3ELi96EEv8GemmArgs:
	s_cmp_ge_u32 s2, 0x100
	s_cbranch_scc1 .Ldn_exit
	s_load_dwordx4 s[4:7], s[0:1], 0x0
	s_load_dwordx2 s[8:9], s[0:1], 0x20
	s_load_dwordx2 s[10:11], s[0:1], 0x38
	s_and_b32 s12, s2, 7
	s_lshr_b32 s13, s2, 3
	s_lshl_b32 s12, s12, 5
	s_add_u32 s12, s12, s13
	s_and_b32 s13, s12, 3
	s_lshr_b32 s12, s12, 2
	s_lshl_b32 s12, s12, 7
	s_mul_i32 s13, s13, 0xc0
	v_lshrrev_b32_e32 v1, 6, v0
	v_and_b32_e32 v14, 7, v0
	v_bfe_u32 v15, v0, 4, 3
	v_xor_b32_e32 v14, v14, v15
	v_readfirstlane_b32 s14, v1
	v_lshrrev_b32_e32 v15, 3, v0
	v_mul_u32_u24_e32 v15, 0x1800, v15
	v_lshl_add_u32 v2, v14, 4, v15
	s_mov_b32 s22, 0x30000
	v_add_u32_e32 v3, s22, v2
	v_add_u32_e32 v4, s22, v3
	v_add_u32_e32 v5, s22, v4
	v_add_u32_e32 v6, s22, v5
	v_add_u32_e32 v7, s22, v6
	v_and_b32_e32 v14, 15, v0
	v_bfe_u32 v15, v0, 4, 2
	v_lshrrev_b32_e32 v16, 1, v14
	v_xor_b32_e32 v16, v16, v15
	v_lshlrev_b32_e32 v16, 4, v16
	v_bfe_u32 v17, v0, 7, 1
	v_bfe_u32 v18, v0, 6, 1
	v_lshl_add_u32 v19, v17, 6, v14
	v_lshl_add_u32 v8, v19, 7, v16
	v_mul_u32_u24_e32 v19, 0x60, v18
	v_add_u32_e32 v19, v19, v14
	v_lshl_add_u32 v9, v19, 7, v16
	v_add_u32_e32 v9, 0x4000, v9
	v_lshl_add_u32 v19, v17, 6, v14
	v_add_u32_e32 v19, s12, v19
	v_mul_u32_u24_e32 v19, 0xc00, v19
	v_mul_u32_u24_e32 v60, 0x60, v18
	v_lshl_add_u32 v60, v15, 2, v60
	v_add_u32_e32 v60, s13, v60
	v_lshl_add_u32 v56, v60, 2, v19
	s_mov_b32 s22, 0xc000
	v_add_u32_e32 v57, s22, v56
	v_add_u32_e32 v58, s22, v57
	v_add_u32_e32 v59, s22, v58
	s_waitcnt lgkmcnt(0)
	s_mul_i32 s22, s12, 0x1800
	s_add_u32 s16, s4, s22
	s_addc_u32 s17, s5, 0
	s_mul_i32 s22, s13, 0x1800
	s_add_u32 s18, s6, s22
	s_addc_u32 s19, s7, 0
	s_lshl_b32 s20, s14, 10
	s_mov_b32 s21, 0
	s_add_u32 m0, s20, 0x0
	s_nop 0
	global_load_lds_dwordx4 v2, s[16:17]
	s_add_u32 m0, s20, 0x1000
	s_nop 0
	global_load_lds_dwordx4 v3, s[16:17]
	s_add_u32 m0, s20, 0x2000
	s_nop 0
	global_load_lds_dwordx4 v4, s[16:17]
	s_add_u32 m0, s20, 0x3000
	s_nop 0
	global_load_lds_dwordx4 v5, s[16:17]
	s_add_u32 m0, s20, 0x4000
	s_nop 0
	global_load_lds_dwordx4 v2, s[18:19]
	s_add_u32 m0, s20, 0x5000
	s_nop 0
	global_load_lds_dwordx4 v3, s[18:19]
	s_add_u32 m0, s20, 0x6000
	s_nop 0
	global_load_lds_dwordx4 v4, s[18:19]
	s_add_u32 m0, s20, 0x7000
	s_nop 0
	global_load_lds_dwordx4 v5, s[18:19]
	s_add_u32 m0, s20, 0x8000
	s_nop 0
	global_load_lds_dwordx4 v6, s[18:19]
	s_add_u32 m0, s20, 0x9000
	s_nop 0
	global_load_lds_dwordx4 v7, s[18:19]
	s_add_u32 s16, s16, 0x80
	s_addc_u32 s17, s17, 0
	s_add_u32 s18, s18, 0x80
	s_addc_u32 s19, s19, 0
	s_add_u32 s20, s20, 0xa000
	s_sub_u32 s22, s20, 0x28000
	s_cmp_ge_u32 s20, 0x28000
	s_cselect_b32 s20, s22, s20
	s_add_u32 m0, s20, 0x0
	s_nop 0
	global_load_lds_dwordx4 v2, s[16:17]
	s_add_u32 m0, s20, 0x1000
	s_nop 0
	global_load_lds_dwordx4 v3, s[16:17]
	s_add_u32 m0, s20, 0x2000
	s_nop 0
	global_load_lds_dwordx4 v4, s[16:17]
	s_add_u32 m0, s20, 0x3000
	s_nop 0
	global_load_lds_dwordx4 v5, s[16:17]
	s_add_u32 m0, s20, 0x4000
	s_nop 0
	global_load_lds_dwordx4 v2, s[18:19]
	s_add_u32 m0, s20, 0x5000
	s_nop 0
	global_load_lds_dwordx4 v3, s[18:19]
	s_add_u32 m0, s20, 0x6000
	s_nop 0
	global_load_lds_dwordx4 v4, s[18:19]
	s_add_u32 m0, s20, 0x7000
	s_nop 0
	global_load_lds_dwordx4 v5, s[18:19]
	s_add_u32 m0, s20, 0x8000
	s_nop 0
	global_load_lds_dwordx4 v6, s[18:19]
	s_add_u32 m0, s20, 0x9000
	s_nop 0
	global_load_lds_dwordx4 v7, s[18:19]
	s_add_u32 s16, s16, 0x80
	s_addc_u32 s17, s17, 0
	s_add_u32 s18, s18, 0x80
	s_addc_u32 s19, s19, 0
	s_add_u32 s20, s20, 0xa000
	s_sub_u32 s22, s20, 0x28000
	s_cmp_ge_u32 s20, 0x28000
	s_cselect_b32 s20, s22, s20
	s_add_u32 m0, s20, 0x0
	s_nop 0
	global_load_lds_dwordx4 v2, s[16:17]
	s_add_u32 m0, s20, 0x1000
	s_nop 0
	global_load_lds_dwordx4 v3, s[16:17]
	s_add_u32 m0, s20, 0x2000
	s_nop 0
	global_load_lds_dwordx4 v4, s[16:17]
	s_add_u32 m0, s20, 0x3000
	s_nop 0
	global_load_lds_dwordx4 v5, s[16:17]
	s_add_u32 m0, s20, 0x4000
	s_nop 0
	global_load_lds_dwordx4 v2, s[18:19]
	s_add_u32 m0, s20, 0x5000
	s_nop 0
	global_load_lds_dwordx4 v3, s[18:19]
	s_add_u32 m0, s20, 0x6000
	s_nop 0
	global_load_lds_dwordx4 v4, s[18:19]
	s_add_u32 m0, s20, 0x7000
	s_nop 0
	global_load_lds_dwordx4 v5, s[18:19]
	s_add_u32 m0, s20, 0x8000
	s_nop 0
	global_load_lds_dwordx4 v6, s[18:19]
	s_add_u32 m0, s20, 0x9000
	s_nop 0
	global_load_lds_dwordx4 v7, s[18:19]
	s_add_u32 s16, s16, 0x80
	s_addc_u32 s17, s17, 0
	s_add_u32 s18, s18, 0x80
	s_addc_u32 s19, s19, 0
	s_add_u32 s20, s20, 0xa000
	s_sub_u32 s22, s20, 0x28000
	s_cmp_ge_u32 s20, 0x28000
	s_cselect_b32 s20, s22, s20
	s_add_u32 m0, s20, 0x0
	s_nop 0
	global_load_lds_dwordx4 v2, s[16:17]
	s_add_u32 m0, s20, 0x1000
	s_nop 0
	global_load_lds_dwordx4 v3, s[16:17]
	s_add_u32 m0, s20, 0x2000
	s_nop 0
	global_load_lds_dwordx4 v4, s[16:17]
	s_add_u32 m0, s20, 0x3000
	s_nop 0
	global_load_lds_dwordx4 v5, s[16:17]
	s_add_u32 m0, s20, 0x4000
	s_nop 0
	global_load_lds_dwordx4 v2, s[18:19]
	v_mov_b32_e32 v64, 0
	v_mov_b32_e32 v65, 0
	v_mov_b32_e32 v66, 0
	v_mov_b32_e32 v67, 0
	v_mov_b32_e32 v68, 0
	v_mov_b32_e32 v69, 0
	v_mov_b32_e32 v70, 0
	v_mov_b32_e32 v71, 0
	v_mov_b32_e32 v72, 0
	v_mov_b32_e32 v73, 0
	v_mov_b32_e32 v74, 0
	v_mov_b32_e32 v75, 0
	v_mov_b32_e32 v76, 0
	v_mov_b32_e32 v77, 0
	v_mov_b32_e32 v78, 0
	v_mov_b32_e32 v79, 0
	v_mov_b32_e32 v80, 0
	v_mov_b32_e32 v81, 0
	v_mov_b32_e32 v82, 0
	v_mov_b32_e32 v83, 0
	v_mov_b32_e32 v84, 0
	v_mov_b32_e32 v85, 0
	v_mov_b32_e32 v86, 0
	v_mov_b32_e32 v87, 0
	v_mov_b32_e32 v88, 0
	v_mov_b32_e32 v89, 0
	v_mov_b32_e32 v90, 0
	v_mov_b32_e32 v91, 0
	v_mov_b32_e32 v92, 0
	v_mov_b32_e32 v93, 0
	v_mov_b32_e32 v94, 0
	v_mov_b32_e32 v95, 0
	v_mov_b32_e32 v96, 0
	v_mov_b32_e32 v97, 0
	v_mov_b32_e32 v98, 0
	v_mov_b32_e32 v99, 0
	v_mov_b32_e32 v100, 0
	v_mov_b32_e32 v101, 0
	v_mov_b32_e32 v102, 0
	v_mov_b32_e32 v103, 0
	v_mov_b32_e32 v104, 0
	v_mov_b32_e32 v105, 0
	v_mov_b32_e32 v106, 0
	v_mov_b32_e32 v107, 0
	v_mov_b32_e32 v108, 0
	v_mov_b32_e32 v109, 0
	v_mov_b32_e32 v110, 0
	v_mov_b32_e32 v111, 0
	v_mov_b32_e32 v112, 0
	v_mov_b32_e32 v113, 0
	v_mov_b32_e32 v114, 0
	v_mov_b32_e32 v115, 0
	v_mov_b32_e32 v116, 0
	v_mov_b32_e32 v117, 0
	v_mov_b32_e32 v118, 0
	v_mov_b32_e32 v119, 0
	v_mov_b32_e32 v120, 0
	v_mov_b32_e32 v121, 0
	v_mov_b32_e32 v122, 0
	v_mov_b32_e32 v123, 0
	v_mov_b32_e32 v124, 0
	v_mov_b32_e32 v125, 0
	v_mov_b32_e32 v126, 0
	v_mov_b32_e32 v127, 0
	v_mov_b32_e32 v128, 0
	v_mov_b32_e32 v129, 0
	v_mov_b32_e32 v130, 0
	v_mov_b32_e32 v131, 0
	v_mov_b32_e32 v132, 0
	v_mov_b32_e32 v133, 0
	v_mov_b32_e32 v134, 0
	v_mov_b32_e32 v135, 0
	v_mov_b32_e32 v136, 0
	v_mov_b32_e32 v137, 0
	v_mov_b32_e32 v138, 0
	v_mov_b32_e32 v139, 0
	v_mov_b32_e32 v140, 0
	v_mov_b32_e32 v141, 0
	v_mov_b32_e32 v142, 0
	v_mov_b32_e32 v143, 0
	v_mov_b32_e32 v144, 0
	v_mov_b32_e32 v145, 0
	v_mov_b32_e32 v146, 0
	v_mov_b32_e32 v147, 0
	v_mov_b32_e32 v148, 0
	v_mov_b32_e32 v149, 0
	v_mov_b32_e32 v150, 0
	v_mov_b32_e32 v151, 0
	v_mov_b32_e32 v152, 0
	v_mov_b32_e32 v153, 0
	v_mov_b32_e32 v154, 0
	v_mov_b32_e32 v155, 0
	v_mov_b32_e32 v156, 0
	v_mov_b32_e32 v157, 0
	v_mov_b32_e32 v158, 0
	v_mov_b32_e32 v159, 0
	s_waitcnt vmcnt(25)
	s_barrier
	v_add_u32_e32 v10, s21, v8
	v_add_u32_e32 v12, s21, v9
	v_xor_b32_e32 v11, 64, v10
	v_xor_b32_e32 v13, 64, v12
	s_add_u32 s21, s21, 0xa000
	s_sub_u32 s23, s21, 0x28000
	s_cmp_ge_u32 s21, 0x28000
	s_cselect_b32 s21, s23, s21
	ds_read_b128 v[160:163], v10 offset:0
	ds_read_b128 v[164:167], v10 offset:2048
	ds_read_b128 v[168:171], v10 offset:4096
	ds_read_b128 v[172:175], v10 offset:6144
	ds_read_b128 v[176:179], v12 offset:0
	ds_read_b128 v[180:183], v12 offset:2048
	ds_read_b128 v[184:187], v12 offset:4096
	ds_read_b128 v[188:191], v12 offset:6144
	ds_read_b128 v[192:195], v12 offset:8192
	ds_read_b128 v[196:199], v12 offset:10240
	ds_read_b128 v[200:203], v11 offset:0
	ds_read_b128 v[204:207], v11 offset:2048
	ds_read_b128 v[208:211], v11 offset:4096
	ds_read_b128 v[212:215], v11 offset:6144
	ds_read_b128 v[216:219], v13 offset:0
	ds_read_b128 v[220:223], v13 offset:2048
	ds_read_b128 v[224:227], v13 offset:4096
	ds_read_b128 v[228:231], v13 offset:6144
	ds_read_b128 v[232:235], v13 offset:8192
	ds_read_b128 v[236:239], v13 offset:10240
	s_mov_b32 s15, 0
.Ldn_loop:
	s_waitcnt lgkmcnt(10)
	v_mfma_f32_16x16x32_bf16 v[64:67], v[176:179], v[160:163], v[64:67]
	v_mfma_f32_16x16x32_bf16 v[68:71], v[176:179], v[164:167], v[68:71]
	s_add_u32 m0, s20, 0x5000
	v_mfma_f32_16x16x32_bf16 v[72:75], v[176:179], v[168:171], v[72:75]
	v_mfma_f32_16x16x32_bf16 v[76:79], v[176:179], v[172:175], v[76:79]
	global_load_lds_dwordx4 v3, s[18:19]
	v_mfma_f32_16x16x32_bf16 v[80:83], v[180:183], v[160:163], v[80:83]
	v_mfma_f32_16x16x32_bf16 v[84:87], v[180:183], v[164:167], v[84:87]
	s_add_u32 m0, s20, 0x6000
	v_mfma_f32_16x16x32_bf16 v[88:91], v[180:183], v[168:171], v[88:91]
	v_mfma_f32_16x16x32_bf16 v[92:95], v[180:183], v[172:175], v[92:95]
	global_load_lds_dwordx4 v4, s[18:19]
	v_mfma_f32_16x16x32_bf16 v[96:99], v[184:187], v[160:163], v[96:99]
	v_mfma_f32_16x16x32_bf16 v[100:103], v[184:187], v[164:167], v[100:103]
	s_add_u32 m0, s20, 0x7000
	v_mfma_f32_16x16x32_bf16 v[104:107], v[184:187], v[168:171], v[104:107]
	v_mfma_f32_16x16x32_bf16 v[108:111], v[184:187], v[172:175], v[108:111]
	global_load_lds_dwordx4 v5, s[18:19]
	v_mfma_f32_16x16x32_bf16 v[112:115], v[188:191], v[160:163], v[112:115]
	v_mfma_f32_16x16x32_bf16 v[116:119], v[188:191], v[164:167], v[116:119]
	s_add_u32 m0, s20, 0x8000
	v_mfma_f32_16x16x32_bf16 v[120:123], v[188:191], v[168:171], v[120:123]
	v_mfma_f32_16x16x32_bf16 v[124:127], v[188:191], v[172:175], v[124:127]
	global_load_lds_dwordx4 v6, s[18:19]
	v_mfma_f32_16x16x32_bf16 v[128:131], v[192:195], v[160:163], v[128:131]
	v_mfma_f32_16x16x32_bf16 v[132:135], v[192:195], v[164:167], v[132:135]
	s_add_u32 m0, s20, 0x9000
	v_mfma_f32_16x16x32_bf16 v[136:139], v[192:195], v[168:171], v[136:139]
	v_mfma_f32_16x16x32_bf16 v[140:143], v[192:195], v[172:175], v[140:143]
	global_load_lds_dwordx4 v7, s[18:19]
	v_mfma_f32_16x16x32_bf16 v[144:147], v[196:199], v[160:163], v[144:147]
	v_mfma_f32_16x16x32_bf16 v[148:151], v[196:199], v[164:167], v[148:151]
	v_mfma_f32_16x16x32_bf16 v[152:155], v[196:199], v[168:171], v[152:155]
	v_mfma_f32_16x16x32_bf16 v[156:159], v[196:199], v[172:175], v[156:159]
	s_add_u32 s16, s16, 0x80
	s_addc_u32 s17, s17, 0
	s_add_u32 s18, s18, 0x80
	s_addc_u32 s19, s19, 0
	s_add_u32 s20, s20, 0xa000
	s_sub_u32 s22, s20, 0x28000
	s_cmp_ge_u32 s20, 0x28000
	s_cselect_b32 s20, s22, s20
	v_add_u32_e32 v10, s21, v8
	v_add_u32_e32 v12, s21, v9
	v_xor_b32_e32 v11, 64, v10
	v_xor_b32_e32 v13, 64, v12
	s_add_u32 s21, s21, 0xa000
	s_sub_u32 s23, s21, 0x28000
	s_cmp_ge_u32 s21, 0x28000
	s_cselect_b32 s21, s23, s21
	s_waitcnt vmcnt(20) lgkmcnt(0)
	s_barrier
	v_mfma_f32_16x16x32_bf16 v[64:67], v[216:219], v[200:203], v[64:67]
	ds_read_b128 v[160:163], v10 offset:0
	v_mfma_f32_16x16x32_bf16 v[68:71], v[216:219], v[204:207], v[68:71]
	s_add_u32 m0, s20, 0x0
	v_mfma_f32_16x16x32_bf16 v[72:75], v[216:219], v[208:211], v[72:75]
	ds_read_b128 v[164:167], v10 offset:2048
	v_mfma_f32_16x16x32_bf16 v[76:79], v[216:219], v[212:215], v[76:79]
	global_load_lds_dwordx4 v2, s[16:17]
	v_mfma_f32_16x16x32_bf16 v[80:83], v[220:223], v[200:203], v[80:83]
	ds_read_b128 v[168:171], v10 offset:4096
	v_mfma_f32_16x16x32_bf16 v[84:87], v[220:223], v[204:207], v[84:87]
	s_add_u32 m0, s20, 0x1000
	v_mfma_f32_16x16x32_bf16 v[88:91], v[220:223], v[208:211], v[88:91]
	ds_read_b128 v[172:175], v10 offset:6144
	v_mfma_f32_16x16x32_bf16 v[92:95], v[220:223], v[212:215], v[92:95]
	global_load_lds_dwordx4 v3, s[16:17]
	v_mfma_f32_16x16x32_bf16 v[96:99], v[224:227], v[200:203], v[96:99]
	ds_read_b128 v[176:179], v12 offset:0
	v_mfma_f32_16x16x32_bf16 v[100:103], v[224:227], v[204:207], v[100:103]
	s_add_u32 m0, s20, 0x2000
	v_mfma_f32_16x16x32_bf16 v[104:107], v[224:227], v[208:211], v[104:107]
	ds_read_b128 v[180:183], v12 offset:2048
	v_mfma_f32_16x16x32_bf16 v[108:111], v[224:227], v[212:215], v[108:111]
	global_load_lds_dwordx4 v4, s[16:17]
	v_mfma_f32_16x16x32_bf16 v[112:115], v[228:231], v[200:203], v[112:115]
	ds_read_b128 v[184:187], v12 offset:4096
	v_mfma_f32_16x16x32_bf16 v[116:119], v[228:231], v[204:207], v[116:119]
	s_add_u32 m0, s20, 0x3000
	v_mfma_f32_16x16x32_bf16 v[120:123], v[228:231], v[208:211], v[120:123]
	ds_read_b128 v[188:191], v12 offset:6144
	v_mfma_f32_16x16x32_bf16 v[124:127], v[228:231], v[212:215], v[124:127]
	global_load_lds_dwordx4 v5, s[16:17]
	v_mfma_f32_16x16x32_bf16 v[128:131], v[232:235], v[200:203], v[128:131]
	ds_read_b128 v[192:195], v12 offset:8192
	v_mfma_f32_16x16x32_bf16 v[132:135], v[232:235], v[204:207], v[132:135]
	s_add_u32 m0, s20, 0x4000
	v_mfma_f32_16x16x32_bf16 v[136:139], v[232:235], v[208:211], v[136:139]
	ds_read_b128 v[196:199], v12 offset:10240
	v_mfma_f32_16x16x32_bf16 v[140:143], v[232:235], v[212:215], v[140:143]
	global_load_lds_dwordx4 v2, s[18:19]
	v_mfma_f32_16x16x32_bf16 v[144:147], v[236:239], v[200:203], v[144:147]
	v_mfma_f32_16x16x32_bf16 v[148:151], v[236:239], v[204:207], v[148:151]
	v_mfma_f32_16x16x32_bf16 v[152:155], v[236:239], v[208:211], v[152:155]
	v_mfma_f32_16x16x32_bf16 v[156:159], v[236:239], v[212:215], v[156:159]
	ds_read_b128 v[200:203], v11 offset:0
	ds_read_b128 v[204:207], v11 offset:2048
	ds_read_b128 v[208:211], v11 offset:4096
	ds_read_b128 v[212:215], v11 offset:6144
	ds_read_b128 v[216:219], v13 offset:0
	ds_read_b128 v[220:223], v13 offset:2048
	ds_read_b128 v[224:227], v13 offset:4096
	ds_read_b128 v[228:231], v13 offset:6144
	ds_read_b128 v[232:235], v13 offset:8192
	ds_read_b128 v[236:239], v13 offset:10240
	s_add_u32 s15, s15, 1
	s_cmp_lt_u32 s15, 44
	s_cbranch_scc1 .Ldn_loop
	s_waitcnt lgkmcnt(10)
	v_mfma_f32_16x16x32_bf16 v[64:67], v[176:179], v[160:163], v[64:67]
	v_mfma_f32_16x16x32_bf16 v[68:71], v[176:179], v[164:167], v[68:71]
	s_add_u32 m0, s20, 0x5000
	v_mfma_f32_16x16x32_bf16 v[72:75], v[176:179], v[168:171], v[72:75]
	v_mfma_f32_16x16x32_bf16 v[76:79], v[176:179], v[172:175], v[76:79]
	global_load_lds_dwordx4 v3, s[18:19]
	v_mfma_f32_16x16x32_bf16 v[80:83], v[180:183], v[160:163], v[80:83]
	v_mfma_f32_16x16x32_bf16 v[84:87], v[180:183], v[164:167], v[84:87]
	s_add_u32 m0, s20, 0x6000
	v_mfma_f32_16x16x32_bf16 v[88:91], v[180:183], v[168:171], v[88:91]
	v_mfma_f32_16x16x32_bf16 v[92:95], v[180:183], v[172:175], v[92:95]
	global_load_lds_dwordx4 v4, s[18:19]
	v_mfma_f32_16x16x32_bf16 v[96:99], v[184:187], v[160:163], v[96:99]
	v_mfma_f32_16x16x32_bf16 v[100:103], v[184:187], v[164:167], v[100:103]
	s_add_u32 m0, s20, 0x7000
	v_mfma_f32_16x16x32_bf16 v[104:107], v[184:187], v[168:171], v[104:107]
	v_mfma_f32_16x16x32_bf16 v[108:111], v[184:187], v[172:175], v[108:111]
	global_load_lds_dwordx4 v5, s[18:19]
	v_mfma_f32_16x16x32_bf16 v[112:115], v[188:191], v[160:163], v[112:115]
	v_mfma_f32_16x16x32_bf16 v[116:119], v[188:191], v[164:167], v[116:119]
	s_add_u32 m0, s20, 0x8000
	v_mfma_f32_16x16x32_bf16 v[120:123], v[188:191], v[168:171], v[120:123]
	v_mfma_f32_16x16x32_bf16 v[124:127], v[188:191], v[172:175], v[124:127]
	global_load_lds_dwordx4 v6, s[18:19]
	v_mfma_f32_16x16x32_bf16 v[128:131], v[192:195], v[160:163], v[128:131]
	v_mfma_f32_16x16x32_bf16 v[132:135], v[192:195], v[164:167], v[132:135]
	s_add_u32 m0, s20, 0x9000
	v_mfma_f32_16x16x32_bf16 v[136:139], v[192:195], v[168:171], v[136:139]
	v_mfma_f32_16x16x32_bf16 v[140:143], v[192:195], v[172:175], v[140:143]
	global_load_lds_dwordx4 v7, s[18:19]
	v_mfma_f32_16x16x32_bf16 v[144:147], v[196:199], v[160:163], v[144:147]
	v_mfma_f32_16x16x32_bf16 v[148:151], v[196:199], v[164:167], v[148:151]
	v_mfma_f32_16x16x32_bf16 v[152:155], v[196:199], v[168:171], v[152:155]
	v_mfma_f32_16x16x32_bf16 v[156:159], v[196:199], v[172:175], v[156:159]
	s_add_u32 s16, s16, 0x80
	s_addc_u32 s17, s17, 0
	s_add_u32 s18, s18, 0x80
	s_addc_u32 s19, s19, 0
	s_add_u32 s20, s20, 0xa000
	s_sub_u32 s22, s20, 0x28000
	s_cmp_ge_u32 s20, 0x28000
	s_cselect_b32 s20, s22, s20
	v_add_u32_e32 v10, s21, v8
	v_add_u32_e32 v12, s21, v9
	v_xor_b32_e32 v11, 64, v10
	v_xor_b32_e32 v13, 64, v12
	s_add_u32 s21, s21, 0xa000
	s_sub_u32 s23, s21, 0x28000
	s_cmp_ge_u32 s21, 0x28000
	s_cselect_b32 s21, s23, s21
	s_waitcnt vmcnt(20) lgkmcnt(0)
	s_barrier
	v_mfma_f32_16x16x32_bf16 v[64:67], v[216:219], v[200:203], v[64:67]
	ds_read_b128 v[160:163], v10 offset:0
	v_mfma_f32_16x16x32_bf16 v[68:71], v[216:219], v[204:207], v[68:71]
	ds_read_b128 v[164:167], v10 offset:2048
	v_mfma_f32_16x16x32_bf16 v[72:75], v[216:219], v[208:211], v[72:75]
	ds_read_b128 v[168:171], v10 offset:4096
	v_mfma_f32_16x16x32_bf16 v[76:79], v[216:219], v[212:215], v[76:79]
	ds_read_b128 v[172:175], v10 offset:6144
	v_mfma_f32_16x16x32_bf16 v[80:83], v[220:223], v[200:203], v[80:83]
	ds_read_b128 v[176:179], v12 offset:0
	v_mfma_f32_16x16x32_bf16 v[84:87], v[220:223], v[204:207], v[84:87]
	ds_read_b128 v[180:183], v12 offset:2048
	v_mfma_f32_16x16x32_bf16 v[88:91], v[220:223], v[208:211], v[88:91]
	ds_read_b128 v[184:187], v12 offset:4096
	v_mfma_f32_16x16x32_bf16 v[92:95], v[220:223], v[212:215], v[92:95]
	ds_read_b128 v[188:191], v12 offset:6144
	v_mfma_f32_16x16x32_bf16 v[96:99], v[224:227], v[200:203], v[96:99]
	ds_read_b128 v[192:195], v12 offset:8192
	v_mfma_f32_16x16x32_bf16 v[100:103], v[224:227], v[204:207], v[100:103]
	ds_read_b128 v[196:199], v12 offset:10240
	v_mfma_f32_16x16x32_bf16 v[104:107], v[224:227], v[208:211], v[104:107]
	v_mfma_f32_16x16x32_bf16 v[108:111], v[224:227], v[212:215], v[108:111]
	v_mfma_f32_16x16x32_bf16 v[112:115], v[228:231], v[200:203], v[112:115]
	v_mfma_f32_16x16x32_bf16 v[116:119], v[228:231], v[204:207], v[116:119]
	v_mfma_f32_16x16x32_bf16 v[120:123], v[228:231], v[208:211], v[120:123]
	v_mfma_f32_16x16x32_bf16 v[124:127], v[228:231], v[212:215], v[124:127]
	v_mfma_f32_16x16x32_bf16 v[128:131], v[232:235], v[200:203], v[128:131]
	v_mfma_f32_16x16x32_bf16 v[132:135], v[232:235], v[204:207], v[132:135]
	v_mfma_f32_16x16x32_bf16 v[136:139], v[232:235], v[208:211], v[136:139]
	v_mfma_f32_16x16x32_bf16 v[140:143], v[232:235], v[212:215], v[140:143]
	v_mfma_f32_16x16x32_bf16 v[144:147], v[236:239], v[200:203], v[144:147]
	v_mfma_f32_16x16x32_bf16 v[148:151], v[236:239], v[204:207], v[148:151]
	v_mfma_f32_16x16x32_bf16 v[152:155], v[236:239], v[208:211], v[152:155]
	v_mfma_f32_16x16x32_bf16 v[156:159], v[236:239], v[212:215], v[156:159]
	ds_read_b128 v[200:203], v11 offset:0
	ds_read_b128 v[204:207], v11 offset:2048
	ds_read_b128 v[208:211], v11 offset:4096
	ds_read_b128 v[212:215], v11 offset:6144
	ds_read_b128 v[216:219], v13 offset:0
	ds_read_b128 v[220:223], v13 offset:2048
	ds_read_b128 v[224:227], v13 offset:4096
	ds_read_b128 v[228:231], v13 offset:6144
	ds_read_b128 v[232:235], v13 offset:8192
	ds_read_b128 v[236:239], v13 offset:10240
	s_waitcnt lgkmcnt(10)
	v_mfma_f32_16x16x32_bf16 v[64:67], v[176:179], v[160:163], v[64:67]
	v_mfma_f32_16x16x32_bf16 v[68:71], v[176:179], v[164:167], v[68:71]
	v_mfma_f32_16x16x32_bf16 v[72:75], v[176:179], v[168:171], v[72:75]
	v_mfma_f32_16x16x32_bf16 v[76:79], v[176:179], v[172:175], v[76:79]
	v_mfma_f32_16x16x32_bf16 v[80:83], v[180:183], v[160:163], v[80:83]
	v_mfma_f32_16x16x32_bf16 v[84:87], v[180:183], v[164:167], v[84:87]
	v_mfma_f32_16x16x32_bf16 v[88:91], v[180:183], v[168:171], v[88:91]
	v_mfma_f32_16x16x32_bf16 v[92:95], v[180:183], v[172:175], v[92:95]
	v_mfma_f32_16x16x32_bf16 v[96:99], v[184:187], v[160:163], v[96:99]
	v_mfma_f32_16x16x32_bf16 v[100:103], v[184:187], v[164:167], v[100:103]
	v_mfma_f32_16x16x32_bf16 v[104:107], v[184:187], v[168:171], v[104:107]
	v_mfma_f32_16x16x32_bf16 v[108:111], v[184:187], v[172:175], v[108:111]
	v_mfma_f32_16x16x32_bf16 v[112:115], v[188:191], v[160:163], v[112:115]
	v_mfma_f32_16x16x32_bf16 v[116:119], v[188:191], v[164:167], v[116:119]
	v_mfma_f32_16x16x32_bf16 v[120:123], v[188:191], v[168:171], v[120:123]
	v_mfma_f32_16x16x32_bf16 v[124:127], v[188:191], v[172:175], v[124:127]
	v_mfma_f32_16x16x32_bf16 v[128:131], v[192:195], v[160:163], v[128:131]
	v_mfma_f32_16x16x32_bf16 v[132:135], v[192:195], v[164:167], v[132:135]
	v_mfma_f32_16x16x32_bf16 v[136:139], v[192:195], v[168:171], v[136:139]
	v_mfma_f32_16x16x32_bf16 v[140:143], v[192:195], v[172:175], v[140:143]
	v_mfma_f32_16x16x32_bf16 v[144:147], v[196:199], v[160:163], v[144:147]
	v_mfma_f32_16x16x32_bf16 v[148:151], v[196:199], v[164:167], v[148:151]
	v_mfma_f32_16x16x32_bf16 v[152:155], v[196:199], v[168:171], v[152:155]
	v_mfma_f32_16x16x32_bf16 v[156:159], v[196:199], v[172:175], v[156:159]
	v_add_u32_e32 v10, s21, v8
	v_add_u32_e32 v12, s21, v9
	v_xor_b32_e32 v11, 64, v10
	v_xor_b32_e32 v13, 64, v12
	s_add_u32 s21, s21, 0xa000
	s_sub_u32 s23, s21, 0x28000
	s_cmp_ge_u32 s21, 0x28000
	s_cselect_b32 s21, s23, s21
	s_waitcnt vmcnt(10) lgkmcnt(0)
	s_barrier
	v_mfma_f32_16x16x32_bf16 v[64:67], v[216:219], v[200:203], v[64:67]
	ds_read_b128 v[160:163], v10 offset:0
	v_mfma_f32_16x16x32_bf16 v[68:71], v[216:219], v[204:207], v[68:71]
	ds_read_b128 v[164:167], v10 offset:2048
	v_mfma_f32_16x16x32_bf16 v[72:75], v[216:219], v[208:211], v[72:75]
	ds_read_b128 v[168:171], v10 offset:4096
	v_mfma_f32_16x16x32_bf16 v[76:79], v[216:219], v[212:215], v[76:79]
	ds_read_b128 v[172:175], v10 offset:6144
	v_mfma_f32_16x16x32_bf16 v[80:83], v[220:223], v[200:203], v[80:83]
	ds_read_b128 v[176:179], v12 offset:0
	v_mfma_f32_16x16x32_bf16 v[84:87], v[220:223], v[204:207], v[84:87]
	ds_read_b128 v[180:183], v12 offset:2048
	v_mfma_f32_16x16x32_bf16 v[88:91], v[220:223], v[208:211], v[88:91]
	ds_read_b128 v[184:187], v12 offset:4096
	v_mfma_f32_16x16x32_bf16 v[92:95], v[220:223], v[212:215], v[92:95]
	ds_read_b128 v[188:191], v12 offset:6144
	v_mfma_f32_16x16x32_bf16 v[96:99], v[224:227], v[200:203], v[96:99]
	ds_read_b128 v[192:195], v12 offset:8192
	v_mfma_f32_16x16x32_bf16 v[100:103], v[224:227], v[204:207], v[100:103]
	ds_read_b128 v[196:199], v12 offset:10240
	v_mfma_f32_16x16x32_bf16 v[104:107], v[224:227], v[208:211], v[104:107]
	v_mfma_f32_16x16x32_bf16 v[108:111], v[224:227], v[212:215], v[108:111]
	v_mfma_f32_16x16x32_bf16 v[112:115], v[228:231], v[200:203], v[112:115]
	v_mfma_f32_16x16x32_bf16 v[116:119], v[228:231], v[204:207], v[116:119]
	v_mfma_f32_16x16x32_bf16 v[120:123], v[228:231], v[208:211], v[120:123]
	v_mfma_f32_16x16x32_bf16 v[124:127], v[228:231], v[212:215], v[124:127]
	v_mfma_f32_16x16x32_bf16 v[128:131], v[232:235], v[200:203], v[128:131]
	v_mfma_f32_16x16x32_bf16 v[132:135], v[232:235], v[204:207], v[132:135]
	v_mfma_f32_16x16x32_bf16 v[136:139], v[232:235], v[208:211], v[136:139]
	v_mfma_f32_16x16x32_bf16 v[140:143], v[232:235], v[212:215], v[140:143]
	v_mfma_f32_16x16x32_bf16 v[144:147], v[236:239], v[200:203], v[144:147]
	v_mfma_f32_16x16x32_bf16 v[148:151], v[236:239], v[204:207], v[148:151]
	v_mfma_f32_16x16x32_bf16 v[152:155], v[236:239], v[208:211], v[152:155]
	v_mfma_f32_16x16x32_bf16 v[156:159], v[236:239], v[212:215], v[156:159]
	ds_read_b128 v[200:203], v11 offset:0
	ds_read_b128 v[204:207], v11 offset:2048
	ds_read_b128 v[208:211], v11 offset:4096
	ds_read_b128 v[212:215], v11 offset:6144
	ds_read_b128 v[216:219], v13 offset:0
	ds_read_b128 v[220:223], v13 offset:2048
	ds_read_b128 v[224:227], v13 offset:4096
	ds_read_b128 v[228:231], v13 offset:6144
	ds_read_b128 v[232:235], v13 offset:8192
	ds_read_b128 v[236:239], v13 offset:10240
	s_waitcnt lgkmcnt(10)
	v_mfma_f32_16x16x32_bf16 v[64:67], v[176:179], v[160:163], v[64:67]
	v_mfma_f32_16x16x32_bf16 v[68:71], v[176:179], v[164:167], v[68:71]
	v_mfma_f32_16x16x32_bf16 v[72:75], v[176:179], v[168:171], v[72:75]
	v_mfma_f32_16x16x32_bf16 v[76:79], v[176:179], v[172:175], v[76:79]
	v_mfma_f32_16x16x32_bf16 v[80:83], v[180:183], v[160:163], v[80:83]
	v_mfma_f32_16x16x32_bf16 v[84:87], v[180:183], v[164:167], v[84:87]
	v_mfma_f32_16x16x32_bf16 v[88:91], v[180:183], v[168:171], v[88:91]
	v_mfma_f32_16x16x32_bf16 v[92:95], v[180:183], v[172:175], v[92:95]
	v_mfma_f32_16x16x32_bf16 v[96:99], v[184:187], v[160:163], v[96:99]
	v_mfma_f32_16x16x32_bf16 v[100:103], v[184:187], v[164:167], v[100:103]
	v_mfma_f32_16x16x32_bf16 v[104:107], v[184:187], v[168:171], v[104:107]
	v_mfma_f32_16x16x32_bf16 v[108:111], v[184:187], v[172:175], v[108:111]
	v_mfma_f32_16x16x32_bf16 v[112:115], v[188:191], v[160:163], v[112:115]
	v_mfma_f32_16x16x32_bf16 v[116:119], v[188:191], v[164:167], v[116:119]
	v_mfma_f32_16x16x32_bf16 v[120:123], v[188:191], v[168:171], v[120:123]
	v_mfma_f32_16x16x32_bf16 v[124:127], v[188:191], v[172:175], v[124:127]
	v_mfma_f32_16x16x32_bf16 v[128:131], v[192:195], v[160:163], v[128:131]
	v_mfma_f32_16x16x32_bf16 v[132:135], v[192:195], v[164:167], v[132:135]
	v_mfma_f32_16x16x32_bf16 v[136:139], v[192:195], v[168:171], v[136:139]
	v_mfma_f32_16x16x32_bf16 v[140:143], v[192:195], v[172:175], v[140:143]
	v_mfma_f32_16x16x32_bf16 v[144:147], v[196:199], v[160:163], v[144:147]
	v_mfma_f32_16x16x32_bf16 v[148:151], v[196:199], v[164:167], v[148:151]
	v_mfma_f32_16x16x32_bf16 v[152:155], v[196:199], v[168:171], v[152:155]
	v_mfma_f32_16x16x32_bf16 v[156:159], v[196:199], v[172:175], v[156:159]
	v_add_u32_e32 v10, s21, v8
	v_add_u32_e32 v12, s21, v9
	v_xor_b32_e32 v11, 64, v10
	v_xor_b32_e32 v13, 64, v12
	s_add_u32 s21, s21, 0xa000
	s_sub_u32 s23, s21, 0x28000
	s_cmp_ge_u32 s21, 0x28000
	s_cselect_b32 s21, s23, s21
	s_waitcnt vmcnt(0) lgkmcnt(0)
	s_barrier
	v_mfma_f32_16x16x32_bf16 v[64:67], v[216:219], v[200:203], v[64:67]
	ds_read_b128 v[160:163], v10 offset:0
	v_mfma_f32_16x16x32_bf16 v[68:71], v[216:219], v[204:207], v[68:71]
	global_load_dwordx4 v[16:19], v56, s[8:9] offset:0
	v_mfma_f32_16x16x32_bf16 v[72:75], v[216:219], v[208:211], v[72:75]
	ds_read_b128 v[164:167], v10 offset:2048
	v_mfma_f32_16x16x32_bf16 v[76:79], v[216:219], v[212:215], v[76:79]
	global_load_dwordx4 v[20:23], v57, s[8:9] offset:0
	v_mfma_f32_16x16x32_bf16 v[80:83], v[220:223], v[200:203], v[80:83]
	ds_read_b128 v[168:171], v10 offset:4096
	v_mfma_f32_16x16x32_bf16 v[84:87], v[220:223], v[204:207], v[84:87]
	global_load_dwordx4 v[24:27], v58, s[8:9] offset:0
	v_mfma_f32_16x16x32_bf16 v[88:91], v[220:223], v[208:211], v[88:91]
	ds_read_b128 v[172:175], v10 offset:6144
	v_mfma_f32_16x16x32_bf16 v[92:95], v[220:223], v[212:215], v[92:95]
	global_load_dwordx4 v[28:31], v59, s[8:9] offset:0
	v_mfma_f32_16x16x32_bf16 v[96:99], v[224:227], v[200:203], v[96:99]
	ds_read_b128 v[176:179], v12 offset:0
	v_mfma_f32_16x16x32_bf16 v[100:103], v[224:227], v[204:207], v[100:103]
	global_load_dwordx4 v[32:35], v56, s[8:9] offset:64
	v_mfma_f32_16x16x32_bf16 v[104:107], v[224:227], v[208:211], v[104:107]
	ds_read_b128 v[180:183], v12 offset:2048
	v_mfma_f32_16x16x32_bf16 v[108:111], v[224:227], v[212:215], v[108:111]
	global_load_dwordx4 v[36:39], v57, s[8:9] offset:64
	v_mfma_f32_16x16x32_bf16 v[112:115], v[228:231], v[200:203], v[112:115]
	ds_read_b128 v[184:187], v12 offset:4096
	v_mfma_f32_16x16x32_bf16 v[116:119], v[228:231], v[204:207], v[116:119]
	global_load_dwordx4 v[40:43], v58, s[8:9] offset:64
	v_mfma_f32_16x16x32_bf16 v[120:123], v[228:231], v[208:211], v[120:123]
	ds_read_b128 v[188:191], v12 offset:6144
	v_mfma_f32_16x16x32_bf16 v[124:127], v[228:231], v[212:215], v[124:127]
	global_load_dwordx4 v[44:47], v59, s[8:9] offset:64
	v_mfma_f32_16x16x32_bf16 v[128:131], v[232:235], v[200:203], v[128:131]
	ds_read_b128 v[192:195], v12 offset:8192
	v_mfma_f32_16x16x32_bf16 v[132:135], v[232:235], v[204:207], v[132:135]
	global_load_dwordx4 v[48:51], v56, s[8:9] offset:128
	v_mfma_f32_16x16x32_bf16 v[136:139], v[232:235], v[208:211], v[136:139]
	ds_read_b128 v[196:199], v12 offset:10240
	v_mfma_f32_16x16x32_bf16 v[140:143], v[232:235], v[212:215], v[140:143]
	global_load_dwordx4 v[52:55], v57, s[8:9] offset:128
	v_mfma_f32_16x16x32_bf16 v[144:147], v[236:239], v[200:203], v[144:147]
	global_load_dwordx4 v[240:243], v58, s[8:9] offset:128
	v_mfma_f32_16x16x32_bf16 v[148:151], v[236:239], v[204:207], v[148:151]
	global_load_dwordx4 v[244:247], v59, s[8:9] offset:128
	v_mfma_f32_16x16x32_bf16 v[152:155], v[236:239], v[208:211], v[152:155]
	global_load_dwordx4 v[248:251], v56, s[8:9] offset:192
	v_mfma_f32_16x16x32_bf16 v[156:159], v[236:239], v[212:215], v[156:159]
	global_load_dwordx4 v[252:255], v57, s[8:9] offset:192
	ds_read_b128 v[200:203], v11 offset:0
	ds_read_b128 v[204:207], v11 offset:2048
	ds_read_b128 v[208:211], v11 offset:4096
	ds_read_b128 v[212:215], v11 offset:6144
	ds_read_b128 v[216:219], v13 offset:0
	ds_read_b128 v[220:223], v13 offset:2048
	ds_read_b128 v[224:227], v13 offset:4096
	ds_read_b128 v[228:231], v13 offset:6144
	ds_read_b128 v[232:235], v13 offset:8192
	ds_read_b128 v[236:239], v13 offset:10240
	s_waitcnt lgkmcnt(10)
	v_mfma_f32_16x16x32_bf16 v[64:67], v[176:179], v[160:163], v[64:67]
	v_mfma_f32_16x16x32_bf16 v[68:71], v[176:179], v[164:167], v[68:71]
	v_mfma_f32_16x16x32_bf16 v[72:75], v[176:179], v[168:171], v[72:75]
	v_mfma_f32_16x16x32_bf16 v[76:79], v[176:179], v[172:175], v[76:79]
	v_mfma_f32_16x16x32_bf16 v[80:83], v[180:183], v[160:163], v[80:83]
	v_mfma_f32_16x16x32_bf16 v[84:87], v[180:183], v[164:167], v[84:87]
	v_mfma_f32_16x16x32_bf16 v[88:91], v[180:183], v[168:171], v[88:91]
	v_mfma_f32_16x16x32_bf16 v[92:95], v[180:183], v[172:175], v[92:95]
	v_mfma_f32_16x16x32_bf16 v[96:99], v[184:187], v[160:163], v[96:99]
	v_mfma_f32_16x16x32_bf16 v[100:103], v[184:187], v[164:167], v[100:103]
	v_mfma_f32_16x16x32_bf16 v[104:107], v[184:187], v[168:171], v[104:107]
	v_mfma_f32_16x16x32_bf16 v[108:111], v[184:187], v[172:175], v[108:111]
	v_mfma_f32_16x16x32_bf16 v[112:115], v[188:191], v[160:163], v[112:115]
	v_mfma_f32_16x16x32_bf16 v[116:119], v[188:191], v[164:167], v[116:119]
	v_mfma_f32_16x16x32_bf16 v[120:123], v[188:191], v[168:171], v[120:123]
	v_mfma_f32_16x16x32_bf16 v[124:127], v[188:191], v[172:175], v[124:127]
	v_mfma_f32_16x16x32_bf16 v[128:131], v[192:195], v[160:163], v[128:131]
	v_mfma_f32_16x16x32_bf16 v[132:135], v[192:195], v[164:167], v[132:135]
	v_mfma_f32_16x16x32_bf16 v[136:139], v[192:195], v[168:171], v[136:139]
	v_mfma_f32_16x16x32_bf16 v[140:143], v[192:195], v[172:175], v[140:143]
	v_mfma_f32_16x16x32_bf16 v[144:147], v[196:199], v[160:163], v[144:147]
	v_mfma_f32_16x16x32_bf16 v[148:151], v[196:199], v[164:167], v[148:151]
	v_mfma_f32_16x16x32_bf16 v[152:155], v[196:199], v[168:171], v[152:155]
	v_mfma_f32_16x16x32_bf16 v[156:159], v[196:199], v[172:175], v[156:159]
	s_waitcnt lgkmcnt(0)
	v_mfma_f32_16x16x32_bf16 v[64:67], v[216:219], v[200:203], v[64:67]
	v_mfma_f32_16x16x32_bf16 v[68:71], v[216:219], v[204:207], v[68:71]
	global_load_dwordx4 v[160:163], v58, s[8:9] offset:192
	v_mfma_f32_16x16x32_bf16 v[72:75], v[216:219], v[208:211], v[72:75]
	v_mfma_f32_16x16x32_bf16 v[76:79], v[216:219], v[212:215], v[76:79]
	global_load_dwordx4 v[164:167], v59, s[8:9] offset:192
	v_mfma_f32_16x16x32_bf16 v[80:83], v[220:223], v[200:203], v[80:83]
	v_mfma_f32_16x16x32_bf16 v[84:87], v[220:223], v[204:207], v[84:87]
	global_load_dwordx4 v[168:171], v56, s[8:9] offset:256
	v_mfma_f32_16x16x32_bf16 v[88:91], v[220:223], v[208:211], v[88:91]
	v_mfma_f32_16x16x32_bf16 v[92:95], v[220:223], v[212:215], v[92:95]
	global_load_dwordx4 v[172:175], v57, s[8:9] offset:256
	v_mfma_f32_16x16x32_bf16 v[96:99], v[224:227], v[200:203], v[96:99]
	v_mfma_f32_16x16x32_bf16 v[100:103], v[224:227], v[204:207], v[100:103]
	global_load_dwordx4 v[176:179], v58, s[8:9] offset:256
	v_mfma_f32_16x16x32_bf16 v[104:107], v[224:227], v[208:211], v[104:107]
	v_mfma_f32_16x16x32_bf16 v[108:111], v[224:227], v[212:215], v[108:111]
	global_load_dwordx4 v[180:183], v59, s[8:9] offset:256
	v_mfma_f32_16x16x32_bf16 v[112:115], v[228:231], v[200:203], v[112:115]
	v_mfma_f32_16x16x32_bf16 v[116:119], v[228:231], v[204:207], v[116:119]
	global_load_dwordx4 v[184:187], v56, s[8:9] offset:320
	v_mfma_f32_16x16x32_bf16 v[120:123], v[228:231], v[208:211], v[120:123]
	v_mfma_f32_16x16x32_bf16 v[124:127], v[228:231], v[212:215], v[124:127]
	global_load_dwordx4 v[188:191], v57, s[8:9] offset:320
	v_mfma_f32_16x16x32_bf16 v[128:131], v[232:235], v[200:203], v[128:131]
	v_mfma_f32_16x16x32_bf16 v[132:135], v[232:235], v[204:207], v[132:135]
	global_load_dwordx4 v[192:195], v58, s[8:9] offset:320
	v_mfma_f32_16x16x32_bf16 v[136:139], v[232:235], v[208:211], v[136:139]
	v_mfma_f32_16x16x32_bf16 v[140:143], v[232:235], v[212:215], v[140:143]
	global_load_dwordx4 v[196:199], v59, s[8:9] offset:320
	v_mfma_f32_16x16x32_bf16 v[144:147], v[236:239], v[200:203], v[144:147]
	v_mfma_f32_16x16x32_bf16 v[148:151], v[236:239], v[204:207], v[148:151]
	v_mfma_f32_16x16x32_bf16 v[152:155], v[236:239], v[208:211], v[152:155]
	v_mfma_f32_16x16x32_bf16 v[156:159], v[236:239], v[212:215], v[156:159]
	s_waitcnt vmcnt(23)
	v_pk_add_f32 v[64:65], v[64:65], v[16:17]
	v_pk_add_f32 v[66:67], v[66:67], v[18:19]
	global_store_dwordx4 v56, v[64:67], s[10:11] offset:0
	s_waitcnt vmcnt(23)
	v_pk_add_f32 v[68:69], v[68:69], v[20:21]
	v_pk_add_f32 v[70:71], v[70:71], v[22:23]
	global_store_dwordx4 v57, v[68:71], s[10:11] offset:0
	s_waitcnt vmcnt(23)
	v_pk_add_f32 v[72:73], v[72:73], v[24:25]
	v_pk_add_f32 v[74:75], v[74:75], v[26:27]
	global_store_dwordx4 v58, v[72:75], s[10:11] offset:0
	s_waitcnt vmcnt(23)
	v_pk_add_f32 v[76:77], v[76:77], v[28:29]
	v_pk_add_f32 v[78:79], v[78:79], v[30:31]
	global_store_dwordx4 v59, v[76:79], s[10:11] offset:0
	s_waitcnt vmcnt(23)
	v_pk_add_f32 v[80:81], v[80:81], v[32:33]
	v_pk_add_f32 v[82:83], v[82:83], v[34:35]
	global_store_dwordx4 v56, v[80:83], s[10:11] offset:64
	s_waitcnt vmcnt(23)
	v_pk_add_f32 v[84:85], v[84:85], v[36:37]
	v_pk_add_f32 v[86:87], v[86:87], v[38:39]
	global_store_dwordx4 v57, v[84:87], s[10:11] offset:64
	s_waitcnt vmcnt(23)
	v_pk_add_f32 v[88:89], v[88:89], v[40:41]
	v_pk_add_f32 v[90:91], v[90:91], v[42:43]
	global_store_dwordx4 v58, v[88:91], s[10:11] offset:64
	s_waitcnt vmcnt(23)
	v_pk_add_f32 v[92:93], v[92:93], v[44:45]
	v_pk_add_f32 v[94:95], v[94:95], v[46:47]
	global_store_dwordx4 v59, v[92:95], s[10:11] offset:64
	s_waitcnt vmcnt(23)
	v_pk_add_f32 v[96:97], v[96:97], v[48:49]
	v_pk_add_f32 v[98:99], v[98:99], v[50:51]
	global_store_dwordx4 v56, v[96:99], s[10:11] offset:128
	s_waitcnt vmcnt(23)
	v_pk_add_f32 v[100:101], v[100:101], v[52:53]
	v_pk_add_f32 v[102:103], v[102:103], v[54:55]
	global_store_dwordx4 v57, v[100:103], s[10:11] offset:128
	s_waitcnt vmcnt(23)
	v_pk_add_f32 v[104:105], v[104:105], v[240:241]
	v_pk_add_f32 v[106:107], v[106:107], v[242:243]
	global_store_dwordx4 v58, v[104:107], s[10:11] offset:128
	s_waitcnt vmcnt(23)
	v_pk_add_f32 v[108:109], v[108:109], v[244:245]
	v_pk_add_f32 v[110:111], v[110:111], v[246:247]
	global_store_dwordx4 v59, v[108:111], s[10:11] offset:128
	s_waitcnt vmcnt(23)
	v_pk_add_f32 v[112:113], v[112:113], v[248:249]
	v_pk_add_f32 v[114:115], v[114:115], v[250:251]
	global_store_dwordx4 v56, v[112:115], s[10:11] offset:192
	s_waitcnt vmcnt(23)
	v_pk_add_f32 v[116:117], v[116:117], v[252:253]
	v_pk_add_f32 v[118:119], v[118:119], v[254:255]
	global_store_dwordx4 v57, v[116:119], s[10:11] offset:192
	s_waitcnt vmcnt(23)
	v_pk_add_f32 v[120:121], v[120:121], v[160:161]
	v_pk_add_f32 v[122:123], v[122:123], v[162:163]
	global_store_dwordx4 v58, v[120:123], s[10:11] offset:192
	s_waitcnt vmcnt(23)
	v_pk_add_f32 v[124:125], v[124:125], v[164:165]
	v_pk_add_f32 v[126:127], v[126:127], v[166:167]
	global_store_dwordx4 v59, v[124:127], s[10:11] offset:192
	s_waitcnt vmcnt(23)
	v_pk_add_f32 v[128:129], v[128:129], v[168:169]
	v_pk_add_f32 v[130:131], v[130:131], v[170:171]
	global_store_dwordx4 v56, v[128:131], s[10:11] offset:256
	s_waitcnt vmcnt(23)
	v_pk_add_f32 v[132:133], v[132:133], v[172:173]
	v_pk_add_f32 v[134:135], v[134:135], v[174:175]
	global_store_dwordx4 v57, v[132:135], s[10:11] offset:256
	s_waitcnt vmcnt(23)
	v_pk_add_f32 v[136:137], v[136:137], v[176:177]
	v_pk_add_f32 v[138:139], v[138:139], v[178:179]
	global_store_dwordx4 v58, v[136:139], s[10:11] offset:256
	s_waitcnt vmcnt(23)
	v_pk_add_f32 v[140:141], v[140:141], v[180:181]
	v_pk_add_f32 v[142:143], v[142:143], v[182:183]
	global_store_dwordx4 v59, v[140:143], s[10:11] offset:256
	s_waitcnt vmcnt(23)
	v_pk_add_f32 v[144:145], v[144:145], v[184:185]
	v_pk_add_f32 v[146:147], v[146:147], v[186:187]
	global_store_dwordx4 v56, v[144:147], s[10:11] offset:320
	s_waitcnt vmcnt(23)
	v_pk_add_f32 v[148:149], v[148:149], v[188:189]
	v_pk_add_f32 v[150:151], v[150:151], v[190:191]
	global_store_dwordx4 v57, v[148:151], s[10:11] offset:320
	s_waitcnt vmcnt(23)
	v_pk_add_f32 v[152:153], v[152:153], v[192:193]
	v_pk_add_f32 v[154:155], v[154:155], v[194:195]
	global_store_dwordx4 v58, v[152:155], s[10:11] offset:320
	s_waitcnt vmcnt(23)
	v_pk_add_f32 v[156:157], v[156:157], v[196:197]
	v_pk_add_f32 v[158:159], v[158:159], v[198:199]
	global_store_dwordx4 v59, v[156:159], s[10:11] offset:320
